# per-workgroup start stagger (0..31 x s_sleep 2 by XCD-local index) at the head of the eight GEMM phases
# speedup vs baseline: 1.0026x; 1.0026x over previous
.LBB0_104:
	s_cmp_lt_i32 s46, 2
	s_cselect_b64 s[2:3], -1, 0
	s_and_b64 s[56:57], s[2:3], s[6:7]
	s_andn2_b64 vcc, exec, s[56:57]
	s_cbranch_vccnz .LBB0_353
	s_bfe_u32 s2, s96, 0x50003
	s_cmp_eq_u32 s2, 0
	s_cbranch_scc1 .Lstag_done_0
.Lstag_loop_0:
	s_sleep 2
	s_sub_u32 s2, s2, 1
	s_cmp_lg_u32 s2, 0
	s_cbranch_scc1 .Lstag_loop_0
.Lstag_done_0:
	s_mov_b64 s[2:3], s[0:1]
	s_load_dwordx2 s[22:23], s[2:3], 0xc8
	s_and_b32 s2, s96, 7
	s_ashr_i32 s58, s96, 31
	s_mul_hi_i32 s3, s91, s2
	s_mul_i32 s2, s91, s2
	s_add_u32 s8, s2, s96
	s_addc_u32 s9, s3, s58
	v_mov_b64_e32 v[2:3], 0x87f
	v_cmp_gt_i64_e64 s[6:7], s[8:9], v[2:3]
	s_and_b64 vcc, exec, s[6:7]
	s_waitcnt lgkmcnt(0)
	s_cbranch_vccnz .LBB0_107
	s_ashr_i32 s2, s8, 31
	s_lshr_b32 s2, s2, 29
	s_add_i32 s2, s8, s2
	s_ashr_i32 s3, s2, 3
	s_and_b32 s2, s2, -8
	s_sub_i32 s2, s8, s2
	s_cmp_lt_i32 s2, 0
	s_movk_i32 s4, 0x111
	s_cselect_b32 s4, s4, 0x110
	s_mul_i32 s2, s2, s4
	s_add_i32 s2, s2, s3
	s_mul_hi_i32 s3, s2, 0x78787879
	s_lshr_b32 s4, s3, 31
	s_ashr_i32 s3, s3, 6
	s_add_i32 s3, s3, s4
	s_lshl_b32 s4, s3, 3
	s_sub_i32 s5, 0x80, s4
	s_min_i32 s5, s5, 8
	s_abs_i32 s8, s5
	v_cvt_f32_u32_e32 v1, s8
	s_sub_i32 s10, 0, s8
	s_mulk_i32 s3, 0x88
	s_sub_i32 s2, s2, s3
	v_rcp_iflag_f32_e32 v1, v1
	s_abs_i32 s3, s2
	s_xor_b32 s9, s2, s5
	s_ashr_i32 s9, s9, 31
	v_mul_f32_e32 v1, 0x4f7ffffe, v1
	v_cvt_u32_f32_e32 v1, v1
	s_nop 0
	v_readfirstlane_b32 s11, v1
	s_mul_i32 s10, s10, s11
	s_mul_hi_u32 s10, s11, s10
	s_add_i32 s11, s11, s10
	s_mul_hi_u32 s10, s3, s11
	s_mul_i32 s11, s10, s8
	s_sub_i32 s3, s3, s11
	s_add_i32 s11, s10, 1
	s_sub_i32 s12, s3, s8
	s_cmp_ge_u32 s3, s8
	s_cselect_b32 s10, s11, s10
	s_cselect_b32 s3, s12, s3
	s_add_i32 s11, s10, 1
	s_cmp_ge_u32 s3, s8
	s_cselect_b32 s3, s11, s10
	s_xor_b32 s3, s3, s9
	s_sub_i32 s3, s3, s9
	s_mul_i32 s5, s3, s5
	s_sub_i32 s2, s2, s5
	s_add_i32 s43, s4, s2
	s_add_i32 s2, s3, 8
	s_cmp_lt_i32 s3, 8
	s_cselect_b32 s49, s3, s2

.LBB0_689:
	s_cmp_lt_i32 s46, 7
	s_cselect_b64 s[2:3], -1, 0
	s_and_b64 s[12:13], s[2:3], s[6:7]
	s_andn2_b64 vcc, exec, s[12:13]
	s_cbranch_vccnz .LBB0_738
	s_bfe_u32 s2, s96, 0x50003
	s_cmp_eq_u32 s2, 0
	s_cbranch_scc1 .Lstag_done_1

.Lstag_done_1:
	s_mov_b64 s[2:3], s[0:1]
	s_cmpk_lt_i32 s96, 0x400
	s_load_dwordx2 s[8:9], s[2:3], 0xc8
	s_cselect_b64 s[6:7], -1, 0
	s_cmpk_gt_i32 s96, 0x3ff
	v_readfirstlane_b32 s2, v0
	s_waitcnt lgkmcnt(0)
	s_cbranch_scc1 .LBB0_696
	s_ashr_i32 s3, s96, 31
	s_lshr_b32 s3, s3, 29
	s_add_i32 s3, s96, s3
	s_and_b32 s4, s3, -8
	s_sub_i32 s4, s96, s4
	s_cmp_gt_i32 s4, -1
	s_cbranch_scc0 .LBB0_693
	s_lshl_b32 s5, s4, 7
	s_cbranch_execz .LBB0_694
	s_branch .LBB0_695

.LBB0_792:
	s_cmp_lt_i32 s46, 8
	s_cselect_b64 s[2:3], -1, 0
	s_and_b64 s[8:9], s[2:3], s[6:7]
	s_andn2_b64 vcc, exec, s[8:9]
	s_cbranch_vccnz .LBB0_823
	s_bfe_u32 s2, s96, 0x50003
	s_cmp_eq_u32 s2, 0
	s_cbranch_scc1 .Lstag_done_2

.Lstag_done_2:
	s_mov_b64 s[2:3], s[0:1]
	s_load_dwordx2 s[6:7], s[2:3], 0xc8
	s_cmpk_gt_i32 s96, 0xff
	v_readfirstlane_b32 s2, v0
	s_waitcnt lgkmcnt(0)
	s_cbranch_scc1 .LBB0_823
	s_ashr_i32 s3, s96, 31
	s_lshr_b32 s4, s3, 29
	s_add_i32 s4, s96, s4
	s_and_b32 s5, s4, -8
	s_sub_i32 s5, s96, s5
	s_cmp_gt_i32 s5, -1
	s_cbranch_scc0 .LBB0_796
	s_lshl_b32 s14, s5, 5
	s_cbranch_execz .LBB0_797
	s_branch .LBB0_798

.LBB0_943:
	s_cmp_lt_i32 s46, 11
	s_cselect_b64 s[2:3], -1, 0
	s_cmp_gt_i32 s47, 10
	s_cselect_b64 s[4:5], -1, 0
	s_and_b64 s[2:3], s[2:3], s[4:5]
	s_andn2_b64 vcc, exec, s[2:3]
	v_cmp_gt_u32_e64 s[6:7], 32, v0
	s_cbranch_vccnz .LBB0_1031
	s_bfe_u32 s2, s96, 0x50003
	s_cmp_eq_u32 s2, 0
	s_cbranch_scc1 .Lstag_done_3

.Lstag_done_3:
	s_mov_b64 s[2:3], s[0:1]
	s_load_dwordx2 s[22:23], s[2:3], 0xc8
	s_waitcnt lgkmcnt(0)
	s_waitcnt vmcnt(0)
	s_barrier
	s_and_saveexec_b64 s[8:9], s[6:7]
	s_cbranch_execz .LBB0_946
	v_lshlrev_b32_e32 v1, 2, v0
	global_load_dword v2, v1, s[26:27] sc1
	v_add_u32_e32 v1, 0, v1
	v_add_u32_e32 v1, 0x25000, v1
	s_waitcnt vmcnt(0)
	ds_write_b32 v1, v2

.LBB0_1276:
	s_cmp_lt_i32 s46, 14
	s_cselect_b64 s[2:3], -1, 0
	s_and_b64 s[18:19], s[2:3], s[6:7]
	s_andn2_b64 vcc, exec, s[18:19]
	s_cbranch_vccnz .LBB0_1337
	s_bfe_u32 s2, s96, 0x50003
	s_cmp_eq_u32 s2, 0
	s_cbranch_scc1 .Lstag_done_4

.Lstag_done_4:
	s_mov_b64 s[2:3], s[0:1]
	s_load_dwordx2 s[16:17], s[2:3], 0xc8
	s_mul_hi_u32 s2, s96, 0xcccccccd
	s_lshr_b32 s2, s2, 2
	s_mul_i32 s2, s2, 5
	s_sub_i32 s2, s96, s2
	s_ashr_i32 s76, s91, 31
	s_mul_i32 s4, s76, s2
	s_mul_hi_u32 s5, s91, s2
	s_add_i32 s5, s5, s4
	s_mul_i32 s2, s91, s2
	s_ashr_i32 s21, s96, 31
	s_add_u32 s10, s2, s96
	s_addc_u32 s11, s5, s21
	s_waitcnt vmcnt(0)
	v_mov_b64_e32 v[2:3], 0x4ff
	v_cmp_gt_i64_e64 s[6:7], s[10:11], v[2:3]
	s_and_b64 vcc, exec, s[6:7]
	s_waitcnt lgkmcnt(0)
	s_cbranch_vccnz .LBB0_1279
	s_ashr_i32 s2, s10, 31
	s_lshr_b32 s2, s2, 29
	s_add_i32 s2, s10, s2
	s_ashr_i32 s5, s2, 3
	s_and_b32 s2, s2, -8
	s_sub_i32 s2, s10, s2
	s_cmp_lt_i32 s2, 0
	s_movk_i32 s8, 0xa1
	s_cselect_b32 s8, s8, 0xa0
	s_mul_i32 s2, s2, s8
	s_add_i32 s2, s2, s5
	s_mul_hi_i32 s5, s2, 0x66666667
	s_lshr_b32 s8, s5, 31
	s_ashr_i32 s5, s5, 5
	s_add_i32 s5, s5, s8
	s_lshl_b32 s8, s5, 3
	s_sub_i32 s9, 0x80, s8
	s_min_i32 s9, s9, 8
	s_abs_i32 s10, s9
	v_cvt_f32_u32_e32 v1, s10
	s_sub_i32 s12, 0, s10
	s_mulk_i32 s5, 0x50
	s_sub_i32 s2, s2, s5
	v_rcp_iflag_f32_e32 v1, v1
	s_abs_i32 s5, s2
	s_xor_b32 s11, s2, s9
	s_ashr_i32 s11, s11, 31
	v_mul_f32_e32 v1, 0x4f7ffffe, v1
	v_cvt_u32_f32_e32 v1, v1
	s_nop 0
	v_readfirstlane_b32 s13, v1
	s_mul_i32 s12, s12, s13
	s_mul_hi_u32 s12, s13, s12
	s_add_i32 s13, s13, s12
	s_mul_hi_u32 s12, s5, s13
	s_mul_i32 s13, s12, s10
	s_sub_i32 s5, s5, s13
	s_add_i32 s13, s12, 1
	s_sub_i32 s14, s5, s10
	s_cmp_ge_u32 s5, s10
	s_cselect_b32 s12, s13, s12
	s_cselect_b32 s5, s14, s5
	s_add_i32 s13, s12, 1
	s_cmp_ge_u32 s5, s10
	s_cselect_b32 s5, s13, s12
	s_xor_b32 s5, s5, s11
	s_sub_i32 s5, s5, s11
	s_mul_i32 s9, s5, s9
	s_sub_i32 s2, s2, s9
	s_add_i32 s20, s8, s2

.LBB0_1527:
	s_cmp_lt_i32 s46, 16
	s_cselect_b64 s[2:3], -1, 0
	s_and_b64 s[10:11], s[2:3], s[6:7]
	s_andn2_b64 vcc, exec, s[10:11]
	s_cbranch_vccnz .LBB0_1570
	s_bfe_u32 s2, s96, 0x50003
	s_cmp_eq_u32 s2, 0
	s_cbranch_scc1 .Lstag_done_5

.Lstag_done_5:
	s_mov_b64 s[2:3], s[0:1]
	s_cmpk_lt_i32 s96, 0x400
	s_load_dwordx2 s[6:7], s[2:3], 0xc8
	s_cselect_b64 s[8:9], -1, 0
	s_cmpk_gt_i32 s96, 0x3ff
	v_readfirstlane_b32 s2, v0
	s_waitcnt lgkmcnt(0)
	s_cbranch_scc1 .LBB0_1534
	s_ashr_i32 s3, s96, 31
	s_lshr_b32 s3, s3, 29
	s_add_i32 s3, s96, s3
	s_and_b32 s4, s3, -8
	s_sub_i32 s4, s96, s4
	s_cmp_gt_i32 s4, -1
	s_cbranch_scc0 .LBB0_1531
	s_lshl_b32 s5, s4, 7
	s_cbranch_execz .LBB0_1532
	s_branch .LBB0_1533

.LBB0_1624:
	s_cmp_lt_i32 s46, 18
	s_cselect_b64 s[2:3], -1, 0
	s_cmp_gt_i32 s47, 17
	s_cselect_b64 s[4:5], -1, 0
	s_and_b64 s[8:9], s[2:3], s[4:5]
	s_andn2_b64 vcc, exec, s[8:9]
	s_cbranch_vccnz .LBB0_1655
	s_bfe_u32 s2, s96, 0x50003
	s_cmp_eq_u32 s2, 0
	s_cbranch_scc1 .Lstag_done_6

.Lstag_done_6:
	s_mov_b64 s[2:3], s[0:1]
	s_load_dwordx2 s[6:7], s[2:3], 0xc8
	s_cmpk_gt_i32 s96, 0xff
	v_readfirstlane_b32 s2, v0
	s_waitcnt lgkmcnt(0)
	s_cbranch_scc1 .LBB0_1655
	s_ashr_i32 s3, s96, 31
	s_lshr_b32 s4, s3, 29
	s_add_i32 s5, s96, s4
	s_and_b32 s4, s5, -8
	s_sub_i32 s4, s96, s4
	s_cmp_gt_i32 s4, -1
	s_cbranch_scc0 .LBB0_1628
	s_lshl_b32 s14, s4, 5
	s_ashr_i32 s10, s5, 3
	s_cbranch_execz .LBB0_1629
	s_branch .LBB0_1630

.LBB0_1775:
	s_cmp_lt_i32 s46, 21
	s_cselect_b64 s[2:3], -1, 0
	s_cmp_gt_i32 s47, 20
	s_cselect_b64 s[4:5], -1, 0
	s_and_b64 s[2:3], s[2:3], s[4:5]
	s_andn2_b64 vcc, exec, s[2:3]
	s_cbranch_vccnz .LBB0_1863
	s_bfe_u32 s2, s96, 0x50003
	s_cmp_eq_u32 s2, 0
	s_cbranch_scc1 .Lstag_done_7

.Lstag_done_7:
	s_mov_b64 s[2:3], s[0:1]
	s_load_dwordx2 s[22:23], s[2:3], 0xc8
	v_cmp_gt_u32_e32 vcc, 32, v0
	s_waitcnt lgkmcnt(0)
	s_waitcnt vmcnt(0)
	s_barrier
	s_and_saveexec_b64 s[6:7], vcc
	s_cbranch_execz .LBB0_1778
	v_lshlrev_b32_e32 v1, 2, v0
	global_load_dword v2, v1, s[26:27] sc1
	v_add_u32_e32 v1, 0, v1
	v_add_u32_e32 v1, 0x25000, v1
	s_waitcnt vmcnt(0)
	ds_write_b32 v1, v2
